# v90 + the four gather-row index loads of the MoE-up tile prologue issued together and waited once
# speedup vs baseline: 1.0096x; 1.0096x over previous
;     __device__ __forceinline__ bool next(int i, Unit& u) const { u.e = 0; u.r0 = 0; return order_next(i, G, c, nM, nN, u.pm, u.pn); }
;     __device__ __forceinline__ const char* b_ptr(const Gemm& g, const Unit& u) const { return (const char*)g.Bt + (size_t)u.pn * (size_t)BM * g.K * 2; }
;     __device__ __forceinline__ bool next(int i, Unit& u) const { if (!order_next(i, G, c, nM, nN, u.pm, u.pn)) return false; u.e = __builtin_amdgcn_readfirstlane(tile_e[u.pm]); u.r0 = __builtin_amdgcn_readfirstlane(tile_r0[u.pm]); return true; }
;     __device__ __forceinline__ const char* b_ptr(const Gemm& g, const Unit& u) const { return (const char*)g.Bt + ((size_t)u.e * estride + (size_t)u.pn * (size_t)BM * g.K) * 2; }
; #define PG8_GLOAD(dst, u) do { if constexpr (GATHER) { _Pragma("unroll") for (int _h = 0; _h < 2; ++_h) _Pragma("unroll") for (int _i = 0; _i < 2; ++_i) dst[_h][_i] = S.row_off(u, _h * HALF + RA[_i], K); } } while (0)
;     __device__ __forceinline__ unsigned row_off(const Unit& u, int vrow, int K) const {
;         const int idx = u.r0 + vrow; int tok = T; if (idx < ecnt[u.e]) tok = elist[(size_t)u.e * T + idx];
;         return (unsigned)tok * (unsigned)(K * 2);
; template <class Epi, class Sched, bool GATHER, bool FP8 = false>
; __device__ __forceinline__ void gemm_phase(LAS unsigned char* lds, const Gemm g, const Sched& S, const Epi& E) {
;     ...
;         const bool has_next = S.next(ui + 1, nxt);
;         const char* nA = has_next ? (GATHER ? (const char*)g.A : (const char*)g.A + (size_t)nxt.pm * tstep) : cA; const char* nB = has_next ? S.b_ptr(g, nxt) : cB;
;         if constexpr (GATHER) { if (has_next) { PG8_GLOAD(gn, nxt); } else { gn[0][0] = gc[0][0]; gn[0][1] = gc[0][1]; gn[1][0] = gc[1][0]; gn[1][1] = gc[1][1]; } }
.LBB0_1417:
	s_and_b64 vcc, exec, s[0:1]
	v_mov_b32_e32 v207, v182
	v_mov_b32_e32 v208, v184
	v_mov_b32_e32 v205, v180
	v_mov_b32_e32 v206, v209
	s_cbranch_vccnz .LBB0_1427
	s_lshl_b32 s21, s22, 2
	s_add_i32 s21, s21, 0
	s_add_i32 s21, s21, 0x20b00
	v_mov_b32_e32 v2, s21
	ds_read_b32 v4, v2
	s_ashr_i32 s23, s22, 31
	s_lshl_b64 s[30:31], s[22:23], 16
	s_add_u32 s30, s19, s30
	v_add_u32_e32 v2, s60, v1
	s_addc_u32 s31, s33, s31
	s_waitcnt lgkmcnt(0)
	v_cmp_lt_i32_e32 vcc, v2, v4
	v_mov_b32_e32 v205, 0x4000
	v_mov_b32_e32 v206, 0x4000
	s_and_saveexec_b64 s[34:35], vcc
	s_cbranch_execz .LBB0_1420
	v_ashrrev_i32_e32 v3, 31, v2
	v_lshl_add_u64 v[2:3], v[2:3], 2, s[30:31]
	global_load_dword v206, v[2:3], off
.LBB0_1420:
	s_or_b64 exec, exec, s[34:35]
	v_add_u32_e32 v2, s60, v198
	v_cmp_lt_i32_e32 vcc, v2, v4
	s_and_saveexec_b64 s[34:35], vcc
	s_cbranch_execz .LBB0_1422
	v_ashrrev_i32_e32 v3, 31, v2
	v_lshl_add_u64 v[2:3], v[2:3], 2, s[30:31]
	global_load_dword v205, v[2:3], off
.LBB0_1422:
	s_or_b64 exec, exec, s[34:35]
	s_add_i32 s21, s60, 0x80
	v_add_u32_e32 v2, s21, v1
	v_cmp_lt_i32_e32 vcc, v2, v4
	v_mov_b32_e32 v207, 0x4000
	v_mov_b32_e32 v208, 0x4000
	s_and_saveexec_b64 s[34:35], vcc
	s_cbranch_execz .LBB0_1424
	v_ashrrev_i32_e32 v3, 31, v2
	v_lshl_add_u64 v[2:3], v[2:3], 2, s[30:31]
	global_load_dword v208, v[2:3], off
.LBB0_1424:
	s_or_b64 exec, exec, s[34:35]
	v_add_u32_e32 v2, s21, v198
	v_cmp_lt_i32_e32 vcc, v2, v4
	s_and_saveexec_b64 s[34:35], vcc
	s_cbranch_execz .LBB0_1426
	v_ashrrev_i32_e32 v3, 31, v2
	v_lshl_add_u64 v[2:3], v[2:3], 2, s[30:31]
	global_load_dword v207, v[2:3], off
.LBB0_1426:
	s_or_b64 exec, exec, s[34:35]
	s_waitcnt vmcnt(0)
	v_lshlrev_b32_e32 v206, 11, v206
	v_lshlrev_b32_e32 v205, 11, v205
	v_lshlrev_b32_e32 v208, 11, v208
	v_lshlrev_b32_e32 v207, 11, v207
